# MoE K-loops: MFMA block order 1,3,2,4 so blocks sharing the activation fragments run back to back (16 instead of 32 ds_read_b128 per K-tile, weight fragments reloaded per block)
# baseline (speedup 1.0000x reference)
.LBB0_726:
	s_cmp_lg_u64 s[2:3], 0
	s_cbranch_scc1 .Lswp_guE_half
	ds_read_b64_tr_b16 v[162:163], v190 offset:0
	ds_read_b64_tr_b16 v[164:165], v191 offset:0
	ds_read_b64_tr_b16 v[170:171], v192 offset:0
	ds_read_b64_tr_b16 v[172:173], v193 offset:0
	ds_read_b128 v[214:217], v207
	ds_read_b128 v[224:227], v207 offset:2048
	ds_read_b128 v[232:235], v207 offset:4096
	ds_read_b128 v[240:243], v207 offset:6144
	ds_read_b64_tr_b16 v[166:167], v190 offset:8192
	ds_read_b64_tr_b16 v[168:169], v191 offset:8192
	ds_read_b64_tr_b16 v[174:175], v192 offset:8192
	ds_read_b64_tr_b16 v[176:177], v193 offset:8192
	ds_read_b128 v[218:221], v207 offset:1024
	ds_read_b128 v[228:231], v207 offset:3072
	ds_read_b128 v[236:239], v207 offset:5120
	ds_read_b128 v[244:247], v207 offset:7168
	s_add_i32 s38, s4, 2
	s_cmp_eq_u32 s34, 28
	s_cselect_b64 s[4:5], -1, 0
	s_and_b64 s[34:35], s[4:5], exec
	s_cselect_b32 s38, 0, s38
	s_cselect_b32 s34, s23, s37
	s_cselect_b32 s35, s22, s36
	s_cselect_b32 s66, s21, s25
	s_cselect_b32 s67, s20, s24
	s_ashr_i32 s39, s38, 31
	s_lshl_b64 s[40:41], s[38:39], 18
	s_add_u32 s68, s67, s40
	s_addc_u32 s69, s66, s41
	s_add_u32 s40, s35, s40
	s_addc_u32 s41, s34, s41
	s_setprio 1
	s_waitcnt lgkmcnt(11)
	v_mfma_f32_16x16x32_bf16 v[158:161], v[162:165], v[214:217], v[158:161]
	v_mfma_f32_16x16x32_bf16 v[154:157], v[170:173], v[214:217], v[154:157]
	s_waitcnt lgkmcnt(10)
	v_mfma_f32_16x16x32_bf16 v[146:149], v[162:165], v[224:227], v[146:149]
	v_mfma_f32_16x16x32_bf16 v[138:141], v[170:173], v[224:227], v[138:141]
	s_waitcnt lgkmcnt(9)
	v_mfma_f32_16x16x32_bf16 v[130:133], v[162:165], v[232:235], v[130:133]
	v_mfma_f32_16x16x32_bf16 v[122:125], v[170:173], v[232:235], v[122:125]
	s_waitcnt lgkmcnt(8)
	v_mfma_f32_16x16x32_bf16 v[114:117], v[162:165], v[240:243], v[114:117]
	v_mfma_f32_16x16x32_bf16 v[106:109], v[170:173], v[240:243], v[106:109]
	ds_read_b64_tr_b16 v[162:163], v190 offset:16384
	ds_read_b64_tr_b16 v[164:165], v191 offset:16384
	ds_read_b64_tr_b16 v[170:171], v192 offset:16384
	ds_read_b64_tr_b16 v[172:173], v193 offset:16384
	s_waitcnt lgkmcnt(7)
	v_mfma_f32_16x16x32_bf16 v[158:161], v[166:169], v[218:221], v[158:161]
	v_mfma_f32_16x16x32_bf16 v[154:157], v[174:177], v[218:221], v[154:157]
	s_waitcnt lgkmcnt(6)
	v_mfma_f32_16x16x32_bf16 v[146:149], v[166:169], v[228:231], v[146:149]
	v_mfma_f32_16x16x32_bf16 v[138:141], v[174:177], v[228:231], v[138:141]
	s_waitcnt lgkmcnt(5)
	v_mfma_f32_16x16x32_bf16 v[130:133], v[166:169], v[236:239], v[130:133]
	v_mfma_f32_16x16x32_bf16 v[122:125], v[174:177], v[236:239], v[122:125]
	s_waitcnt lgkmcnt(4)
	v_mfma_f32_16x16x32_bf16 v[114:117], v[166:169], v[244:247], v[114:117]
	v_mfma_f32_16x16x32_bf16 v[106:109], v[174:177], v[244:247], v[106:109]
	ds_read_b64_tr_b16 v[166:167], v190 offset:24576
	ds_read_b64_tr_b16 v[168:169], v191 offset:24576
	ds_read_b64_tr_b16 v[174:175], v192 offset:24576
	ds_read_b64_tr_b16 v[176:177], v193 offset:24576
	s_waitcnt lgkmcnt(4)
	v_mfma_f32_16x16x32_bf16 v[150:153], v[162:165], v[214:217], v[150:153]
	v_mfma_f32_16x16x32_bf16 v[142:145], v[170:173], v[214:217], v[142:145]
	ds_read_b128 v[214:217], v207 offset:16384
	v_mfma_f32_16x16x32_bf16 v[134:137], v[162:165], v[224:227], v[134:137]
	v_mfma_f32_16x16x32_bf16 v[126:129], v[170:173], v[224:227], v[126:129]
	ds_read_b128 v[224:227], v207 offset:18432
	v_mfma_f32_16x16x32_bf16 v[118:121], v[162:165], v[232:235], v[118:121]
	v_mfma_f32_16x16x32_bf16 v[110:113], v[170:173], v[232:235], v[110:113]
	ds_read_b128 v[232:235], v207 offset:20480
	v_mfma_f32_16x16x32_bf16 v[102:105], v[162:165], v[240:243], v[102:105]
	v_mfma_f32_16x16x32_bf16 v[98:101], v[170:173], v[240:243], v[98:101]
	ds_read_b128 v[240:243], v207 offset:22528
	ds_read_b64_tr_b16 v[162:163], v190 offset:0
	ds_read_b64_tr_b16 v[164:165], v191 offset:0
	ds_read_b64_tr_b16 v[170:171], v192 offset:0
	ds_read_b64_tr_b16 v[172:173], v193 offset:0
	s_waitcnt lgkmcnt(8)
	v_mfma_f32_16x16x32_bf16 v[150:153], v[166:169], v[218:221], v[150:153]
	v_mfma_f32_16x16x32_bf16 v[142:145], v[174:177], v[218:221], v[142:145]
	ds_read_b128 v[218:221], v207 offset:17408
	v_mfma_f32_16x16x32_bf16 v[134:137], v[166:169], v[228:231], v[134:137]
	v_mfma_f32_16x16x32_bf16 v[126:129], v[174:177], v[228:231], v[126:129]
	ds_read_b128 v[228:231], v207 offset:19456
	v_mfma_f32_16x16x32_bf16 v[118:121], v[166:169], v[236:239], v[118:121]
	v_mfma_f32_16x16x32_bf16 v[110:113], v[174:177], v[236:239], v[110:113]
	ds_read_b128 v[236:239], v207 offset:21504
	v_mfma_f32_16x16x32_bf16 v[102:105], v[166:169], v[244:247], v[102:105]
	v_mfma_f32_16x16x32_bf16 v[98:101], v[174:177], v[244:247], v[98:101]
	ds_read_b128 v[244:247], v207 offset:23552
	ds_read_b64_tr_b16 v[166:167], v190 offset:8192
	ds_read_b64_tr_b16 v[168:169], v191 offset:8192
	ds_read_b64_tr_b16 v[174:175], v192 offset:8192
	ds_read_b64_tr_b16 v[176:177], v193 offset:8192
	s_waitcnt lgkmcnt(8)
	v_mfma_f32_16x16x32_bf16 v[94:97], v[162:165], v[214:217], v[94:97]
	v_mfma_f32_16x16x32_bf16 v[86:89], v[170:173], v[214:217], v[86:89]
	v_mfma_f32_16x16x32_bf16 v[78:81], v[162:165], v[224:227], v[78:81]
	v_mfma_f32_16x16x32_bf16 v[70:73], v[170:173], v[224:227], v[70:73]
	v_mfma_f32_16x16x32_bf16 v[62:65], v[162:165], v[232:235], v[62:65]
	v_mfma_f32_16x16x32_bf16 v[54:57], v[170:173], v[232:235], v[54:57]
	v_mfma_f32_16x16x32_bf16 v[46:49], v[162:165], v[240:243], v[46:49]
	v_mfma_f32_16x16x32_bf16 v[38:41], v[170:173], v[240:243], v[38:41]
	ds_read_b64_tr_b16 v[162:163], v190 offset:16384
	ds_read_b64_tr_b16 v[164:165], v191 offset:16384
	ds_read_b64_tr_b16 v[170:171], v192 offset:16384
	ds_read_b64_tr_b16 v[172:173], v193 offset:16384
	s_waitcnt lgkmcnt(4)
	v_mfma_f32_16x16x32_bf16 v[94:97], v[166:169], v[218:221], v[94:97]
	v_mfma_f32_16x16x32_bf16 v[86:89], v[174:177], v[218:221], v[86:89]
	v_mfma_f32_16x16x32_bf16 v[78:81], v[166:169], v[228:231], v[78:81]
	v_mfma_f32_16x16x32_bf16 v[70:73], v[174:177], v[228:231], v[70:73]
	v_mfma_f32_16x16x32_bf16 v[62:65], v[166:169], v[236:239], v[62:65]
	v_mfma_f32_16x16x32_bf16 v[54:57], v[174:177], v[236:239], v[54:57]
	v_mfma_f32_16x16x32_bf16 v[46:49], v[166:169], v[244:247], v[46:49]
	v_mfma_f32_16x16x32_bf16 v[38:41], v[174:177], v[244:247], v[38:41]
	ds_read_b64_tr_b16 v[166:167], v190 offset:24576
	ds_read_b64_tr_b16 v[168:169], v191 offset:24576
	ds_read_b64_tr_b16 v[174:175], v192 offset:24576
	ds_read_b64_tr_b16 v[176:177], v193 offset:24576
	s_waitcnt lgkmcnt(4)
	v_mfma_f32_16x16x32_bf16 v[90:93], v[162:165], v[214:217], v[90:93]
	v_mfma_f32_16x16x32_bf16 v[82:85], v[170:173], v[214:217], v[82:85]
	s_waitcnt vmcnt(11)
	v_cvt_pk_bf16_f32 v248, v2, v3
	v_cvt_pk_bf16_f32 v249, v4, v5
	ds_write_b64 v199, v[248:249]
	s_add_u32 s70, s40, 0x6000
	s_addc_u32 s71, s41, 0
	global_load_dwordx4 v[2:5], v189, s[70:71]
	v_mfma_f32_16x16x32_bf16 v[74:77], v[162:165], v[224:227], v[74:77]
	v_mfma_f32_16x16x32_bf16 v[66:69], v[170:173], v[224:227], v[66:69]
	s_waitcnt vmcnt(11)
	v_cvt_pk_bf16_f32 v248, v6, v7
	v_cvt_pk_bf16_f32 v249, v8, v9
	ds_write_b64 v200, v[248:249]
	s_add_u32 s72, s40, 0x4000
	s_addc_u32 s73, s41, 0
	global_load_dwordx4 v[6:9], v189, s[72:73]
	v_mfma_f32_16x16x32_bf16 v[58:61], v[162:165], v[232:235], v[58:61]
	v_mfma_f32_16x16x32_bf16 v[50:53], v[170:173], v[232:235], v[50:53]
	s_waitcnt vmcnt(11)
	v_cvt_pk_bf16_f32 v248, v10, v11
	v_cvt_pk_bf16_f32 v249, v12, v13
	ds_write_b64 v201, v[248:249]
	s_add_u32 s70, s68, 0x6000
	s_addc_u32 s71, s69, 0
	global_load_dwordx4 v[10:13], v189, s[70:71]
	v_mfma_f32_16x16x32_bf16 v[42:45], v[162:165], v[240:243], v[42:45]
	v_mfma_f32_16x16x32_bf16 v[30:33], v[170:173], v[240:243], v[30:33]
	s_waitcnt vmcnt(11)
	v_cvt_pk_bf16_f32 v248, v14, v15
	v_cvt_pk_bf16_f32 v249, v16, v17
	ds_write_b64 v202, v[248:249]
	s_add_u32 s72, s40, 0x2000
	s_addc_u32 s73, s41, 0
	global_load_dwordx4 v[14:17], v189, s[72:73]
	s_waitcnt lgkmcnt(4)
	v_mfma_f32_16x16x32_bf16 v[90:93], v[166:169], v[218:221], v[90:93]
	v_mfma_f32_16x16x32_bf16 v[82:85], v[174:177], v[218:221], v[82:85]
	s_waitcnt vmcnt(11)
	v_cvt_pk_bf16_f32 v248, v18, v19
	v_cvt_pk_bf16_f32 v249, v20, v21
	ds_write_b64 v203, v[248:249]
	s_add_u32 s70, s68, 0x4000
	s_addc_u32 s71, s69, 0
	global_load_dwordx4 v[18:21], v189, s[70:71]
	v_mfma_f32_16x16x32_bf16 v[74:77], v[166:169], v[228:231], v[74:77]
	v_mfma_f32_16x16x32_bf16 v[66:69], v[174:177], v[228:231], v[66:69]
	s_waitcnt vmcnt(11)
	v_cvt_pk_bf16_f32 v248, v22, v23
	v_cvt_pk_bf16_f32 v249, v24, v25
	ds_write_b64 v204, v[248:249]
	global_load_dwordx4 v[22:25], v189, s[40:41]
	v_mfma_f32_16x16x32_bf16 v[58:61], v[166:169], v[236:239], v[58:61]
	v_mfma_f32_16x16x32_bf16 v[50:53], v[174:177], v[236:239], v[50:53]
	s_waitcnt vmcnt(11)
	v_cvt_pk_bf16_f32 v248, v26, v27
	v_cvt_pk_bf16_f32 v249, v28, v29
	ds_write_b64 v205, v[248:249]
	s_add_u32 s70, s68, 0x2000
	s_addc_u32 s71, s69, 0
	global_load_dwordx4 v[26:29], v189, s[70:71]
	v_mfma_f32_16x16x32_bf16 v[42:45], v[166:169], v[244:247], v[42:45]
	v_mfma_f32_16x16x32_bf16 v[30:33], v[174:177], v[244:247], v[30:33]
	s_waitcnt vmcnt(11)
	v_cvt_pk_bf16_f32 v248, v34, v35
	v_cvt_pk_bf16_f32 v249, v36, v37
	ds_write_b64 v206, v[248:249]
	global_load_dwordx4 v[34:37], v189, s[68:69]
	s_setprio 0

.LBB0_732:
	s_cmp_lg_u64 s[2:3], 0
	s_cbranch_scc1 .Lswp_guO_half
	ds_read_b64_tr_b16 v[162:163], v190 offset:32768
	ds_read_b64_tr_b16 v[164:165], v191 offset:32768
	ds_read_b64_tr_b16 v[170:171], v192 offset:32768
	ds_read_b64_tr_b16 v[172:173], v193 offset:32768
	ds_read_b128 v[214:217], v207 offset:32768
	ds_read_b128 v[224:227], v207 offset:34816
	ds_read_b128 v[232:235], v207 offset:36864
	ds_read_b128 v[240:243], v207 offset:38912
	ds_read_b64_tr_b16 v[166:167], v190 offset:40960
	ds_read_b64_tr_b16 v[168:169], v191 offset:40960
	ds_read_b64_tr_b16 v[174:175], v192 offset:40960
	ds_read_b64_tr_b16 v[176:177], v193 offset:40960
	ds_read_b128 v[218:221], v207 offset:33792
	ds_read_b128 v[228:231], v207 offset:35840
	ds_read_b128 v[236:239], v207 offset:37888
	ds_read_b128 v[244:247], v207 offset:39936
	s_lshl_b64 s[2:3], s[38:39], 18
	s_add_u32 s4, s2, 0x40000
	s_addc_u32 s5, s3, 0
	s_add_u32 s2, s67, s4
	s_addc_u32 s3, s66, s5
	s_add_u32 s4, s35, s4
	s_addc_u32 s5, s34, s5
	s_setprio 1
	s_waitcnt lgkmcnt(11)
	v_mfma_f32_16x16x32_bf16 v[158:161], v[162:165], v[214:217], v[158:161]
	v_mfma_f32_16x16x32_bf16 v[154:157], v[170:173], v[214:217], v[154:157]
	s_waitcnt lgkmcnt(10)
	v_mfma_f32_16x16x32_bf16 v[146:149], v[162:165], v[224:227], v[146:149]
	v_mfma_f32_16x16x32_bf16 v[138:141], v[170:173], v[224:227], v[138:141]
	s_waitcnt lgkmcnt(9)
	v_mfma_f32_16x16x32_bf16 v[130:133], v[162:165], v[232:235], v[130:133]
	v_mfma_f32_16x16x32_bf16 v[122:125], v[170:173], v[232:235], v[122:125]
	s_waitcnt lgkmcnt(8)
	v_mfma_f32_16x16x32_bf16 v[114:117], v[162:165], v[240:243], v[114:117]
	v_mfma_f32_16x16x32_bf16 v[106:109], v[170:173], v[240:243], v[106:109]
	ds_read_b64_tr_b16 v[162:163], v190 offset:49152
	ds_read_b64_tr_b16 v[164:165], v191 offset:49152
	ds_read_b64_tr_b16 v[170:171], v192 offset:49152
	ds_read_b64_tr_b16 v[172:173], v193 offset:49152
	s_waitcnt lgkmcnt(7)
	v_mfma_f32_16x16x32_bf16 v[158:161], v[166:169], v[218:221], v[158:161]
	v_mfma_f32_16x16x32_bf16 v[154:157], v[174:177], v[218:221], v[154:157]
	s_waitcnt lgkmcnt(6)
	v_mfma_f32_16x16x32_bf16 v[146:149], v[166:169], v[228:231], v[146:149]
	v_mfma_f32_16x16x32_bf16 v[138:141], v[174:177], v[228:231], v[138:141]
	s_waitcnt lgkmcnt(5)
	v_mfma_f32_16x16x32_bf16 v[130:133], v[166:169], v[236:239], v[130:133]
	v_mfma_f32_16x16x32_bf16 v[122:125], v[174:177], v[236:239], v[122:125]
	s_waitcnt lgkmcnt(4)
	v_mfma_f32_16x16x32_bf16 v[114:117], v[166:169], v[244:247], v[114:117]
	v_mfma_f32_16x16x32_bf16 v[106:109], v[174:177], v[244:247], v[106:109]
	ds_read_b64_tr_b16 v[166:167], v190 offset:57344
	ds_read_b64_tr_b16 v[168:169], v191 offset:57344
	ds_read_b64_tr_b16 v[174:175], v192 offset:57344
	ds_read_b64_tr_b16 v[176:177], v193 offset:57344
	s_waitcnt lgkmcnt(4)
	v_mfma_f32_16x16x32_bf16 v[150:153], v[162:165], v[214:217], v[150:153]
	v_mfma_f32_16x16x32_bf16 v[142:145], v[170:173], v[214:217], v[142:145]
	ds_read_b128 v[214:217], v207 offset:49152
	v_mfma_f32_16x16x32_bf16 v[134:137], v[162:165], v[224:227], v[134:137]
	v_mfma_f32_16x16x32_bf16 v[126:129], v[170:173], v[224:227], v[126:129]
	ds_read_b128 v[224:227], v207 offset:51200
	v_mfma_f32_16x16x32_bf16 v[118:121], v[162:165], v[232:235], v[118:121]
	v_mfma_f32_16x16x32_bf16 v[110:113], v[170:173], v[232:235], v[110:113]
	ds_read_b128 v[232:235], v207 offset:53248
	v_mfma_f32_16x16x32_bf16 v[102:105], v[162:165], v[240:243], v[102:105]
	v_mfma_f32_16x16x32_bf16 v[98:101], v[170:173], v[240:243], v[98:101]
	ds_read_b128 v[240:243], v207 offset:55296
	ds_read_b64_tr_b16 v[162:163], v190 offset:32768
	ds_read_b64_tr_b16 v[164:165], v191 offset:32768
	ds_read_b64_tr_b16 v[170:171], v192 offset:32768
	ds_read_b64_tr_b16 v[172:173], v193 offset:32768
	s_waitcnt lgkmcnt(8)
	v_mfma_f32_16x16x32_bf16 v[150:153], v[166:169], v[218:221], v[150:153]
	v_mfma_f32_16x16x32_bf16 v[142:145], v[174:177], v[218:221], v[142:145]
	ds_read_b128 v[218:221], v207 offset:50176
	v_mfma_f32_16x16x32_bf16 v[134:137], v[166:169], v[228:231], v[134:137]
	v_mfma_f32_16x16x32_bf16 v[126:129], v[174:177], v[228:231], v[126:129]
	ds_read_b128 v[228:231], v207 offset:52224
	v_mfma_f32_16x16x32_bf16 v[118:121], v[166:169], v[236:239], v[118:121]
	v_mfma_f32_16x16x32_bf16 v[110:113], v[174:177], v[236:239], v[110:113]
	ds_read_b128 v[236:239], v207 offset:54272
	v_mfma_f32_16x16x32_bf16 v[102:105], v[166:169], v[244:247], v[102:105]
	v_mfma_f32_16x16x32_bf16 v[98:101], v[174:177], v[244:247], v[98:101]
	ds_read_b128 v[244:247], v207 offset:56320
	ds_read_b64_tr_b16 v[166:167], v190 offset:40960
	ds_read_b64_tr_b16 v[168:169], v191 offset:40960
	ds_read_b64_tr_b16 v[174:175], v192 offset:40960
	ds_read_b64_tr_b16 v[176:177], v193 offset:40960
	s_waitcnt lgkmcnt(8)
	v_mfma_f32_16x16x32_bf16 v[94:97], v[162:165], v[214:217], v[94:97]
	v_mfma_f32_16x16x32_bf16 v[86:89], v[170:173], v[214:217], v[86:89]
	v_mfma_f32_16x16x32_bf16 v[78:81], v[162:165], v[224:227], v[78:81]
	v_mfma_f32_16x16x32_bf16 v[70:73], v[170:173], v[224:227], v[70:73]
	v_mfma_f32_16x16x32_bf16 v[62:65], v[162:165], v[232:235], v[62:65]
	v_mfma_f32_16x16x32_bf16 v[54:57], v[170:173], v[232:235], v[54:57]
	v_mfma_f32_16x16x32_bf16 v[46:49], v[162:165], v[240:243], v[46:49]
	v_mfma_f32_16x16x32_bf16 v[38:41], v[170:173], v[240:243], v[38:41]
	ds_read_b64_tr_b16 v[162:163], v190 offset:49152
	ds_read_b64_tr_b16 v[164:165], v191 offset:49152
	ds_read_b64_tr_b16 v[170:171], v192 offset:49152
	ds_read_b64_tr_b16 v[172:173], v193 offset:49152
	s_waitcnt lgkmcnt(4)
	v_mfma_f32_16x16x32_bf16 v[94:97], v[166:169], v[218:221], v[94:97]
	v_mfma_f32_16x16x32_bf16 v[86:89], v[174:177], v[218:221], v[86:89]
	v_mfma_f32_16x16x32_bf16 v[78:81], v[166:169], v[228:231], v[78:81]
	v_mfma_f32_16x16x32_bf16 v[70:73], v[174:177], v[228:231], v[70:73]
	v_mfma_f32_16x16x32_bf16 v[62:65], v[166:169], v[236:239], v[62:65]
	v_mfma_f32_16x16x32_bf16 v[54:57], v[174:177], v[236:239], v[54:57]
	v_mfma_f32_16x16x32_bf16 v[46:49], v[166:169], v[244:247], v[46:49]
	v_mfma_f32_16x16x32_bf16 v[38:41], v[174:177], v[244:247], v[38:41]
	ds_read_b64_tr_b16 v[166:167], v190 offset:57344
	ds_read_b64_tr_b16 v[168:169], v191 offset:57344
	ds_read_b64_tr_b16 v[174:175], v192 offset:57344
	ds_read_b64_tr_b16 v[176:177], v193 offset:57344
	s_waitcnt lgkmcnt(4)
	v_mfma_f32_16x16x32_bf16 v[90:93], v[162:165], v[214:217], v[90:93]
	v_mfma_f32_16x16x32_bf16 v[82:85], v[170:173], v[214:217], v[82:85]
	s_waitcnt vmcnt(9)
	v_cvt_pk_bf16_f32 v248, v2, v3
	v_cvt_pk_bf16_f32 v249, v4, v5
	ds_write_b64 v197, v[248:249] offset:16384
	global_load_dwordx4 v[2:5], v189, s[2:3]
	v_mfma_f32_16x16x32_bf16 v[74:77], v[162:165], v[224:227], v[74:77]
	v_mfma_f32_16x16x32_bf16 v[66:69], v[170:173], v[224:227], v[66:69]
	s_waitcnt vmcnt(9)
	v_cvt_pk_bf16_f32 v248, v6, v7
	v_cvt_pk_bf16_f32 v249, v8, v9
	ds_write_b64 v196, v[248:249] offset:16384
	global_load_dwordx4 v[6:9], v189, s[4:5]
	v_mfma_f32_16x16x32_bf16 v[58:61], v[162:165], v[232:235], v[58:61]
	v_mfma_f32_16x16x32_bf16 v[50:53], v[170:173], v[232:235], v[50:53]
	s_waitcnt vmcnt(9)
	v_cvt_pk_bf16_f32 v248, v10, v11
	v_cvt_pk_bf16_f32 v249, v12, v13
	ds_write_b64 v197, v[248:249]
	s_add_u32 s98, s2, 0x2000
	s_addc_u32 s99, s3, 0
	global_load_dwordx4 v[10:13], v189, s[98:99]
	v_mfma_f32_16x16x32_bf16 v[42:45], v[162:165], v[240:243], v[42:45]
	v_mfma_f32_16x16x32_bf16 v[30:33], v[170:173], v[240:243], v[30:33]
	s_waitcnt vmcnt(9)
	v_cvt_pk_bf16_f32 v248, v14, v15
	v_cvt_pk_bf16_f32 v249, v16, v17
	ds_write_b64 v195, v[248:249] offset:16384
	s_add_u32 s100, s4, 0x2000
	s_addc_u32 s101, s5, 0
	global_load_dwordx4 v[14:17], v189, s[100:101]
	s_waitcnt lgkmcnt(4)
	v_mfma_f32_16x16x32_bf16 v[90:93], v[166:169], v[218:221], v[90:93]
	v_mfma_f32_16x16x32_bf16 v[82:85], v[174:177], v[218:221], v[82:85]
	s_waitcnt vmcnt(9)
	v_cvt_pk_bf16_f32 v248, v18, v19
	v_cvt_pk_bf16_f32 v249, v20, v21
	ds_write_b64 v196, v[248:249]
	s_add_u32 s98, s2, 0x4000
	s_addc_u32 s99, s3, 0
	global_load_dwordx4 v[18:21], v189, s[98:99]
	v_mfma_f32_16x16x32_bf16 v[74:77], v[166:169], v[228:231], v[74:77]
	v_mfma_f32_16x16x32_bf16 v[66:69], v[174:177], v[228:231], v[66:69]
	s_waitcnt vmcnt(9)
	v_cvt_pk_bf16_f32 v248, v22, v23
	v_cvt_pk_bf16_f32 v249, v24, v25
	ds_write_b64 v194, v[248:249] offset:16384
	s_add_u32 s100, s4, 0x4000
	s_addc_u32 s101, s5, 0
	global_load_dwordx4 v[22:25], v189, s[100:101]
	v_mfma_f32_16x16x32_bf16 v[58:61], v[166:169], v[236:239], v[58:61]
	v_mfma_f32_16x16x32_bf16 v[50:53], v[174:177], v[236:239], v[50:53]
	s_waitcnt vmcnt(9)
	v_cvt_pk_bf16_f32 v248, v26, v27
	v_cvt_pk_bf16_f32 v249, v28, v29
	ds_write_b64 v195, v[248:249]
	s_add_u32 s98, s2, 0x6000
	s_addc_u32 s99, s3, 0
	global_load_dwordx4 v[26:29], v189, s[98:99]
	v_mfma_f32_16x16x32_bf16 v[42:45], v[166:169], v[244:247], v[42:45]
	v_mfma_f32_16x16x32_bf16 v[30:33], v[174:177], v[244:247], v[30:33]
	s_waitcnt vmcnt(9)
	v_cvt_pk_bf16_f32 v248, v34, v35
	v_cvt_pk_bf16_f32 v249, v36, v37
	ds_write_b64 v194, v[248:249]
	s_add_u32 s100, s4, 0x6000
	s_addc_u32 s101, s5, 0
	global_load_dwordx4 v[34:37], v189, s[100:101]
	s_setprio 0

.Lswp_guE_half:
	ds_read_b64_tr_b16 v[162:163], v190 offset:0
	ds_read_b64_tr_b16 v[164:165], v191 offset:0
	ds_read_b64_tr_b16 v[170:171], v192 offset:0
	ds_read_b64_tr_b16 v[172:173], v193 offset:0
	ds_read_b128 v[214:217], v207
	ds_read_b128 v[224:227], v207 offset:2048
	ds_read_b128 v[232:235], v207 offset:4096
	ds_read_b128 v[240:243], v207 offset:6144
	ds_read_b64_tr_b16 v[166:167], v190 offset:8192
	ds_read_b64_tr_b16 v[168:169], v191 offset:8192
	ds_read_b64_tr_b16 v[174:175], v192 offset:8192
	ds_read_b64_tr_b16 v[176:177], v193 offset:8192
	ds_read_b128 v[218:221], v207 offset:1024
	ds_read_b128 v[228:231], v207 offset:3072
	ds_read_b128 v[236:239], v207 offset:5120
	ds_read_b128 v[244:247], v207 offset:7168
	s_add_i32 s38, s4, 2
	s_cmp_eq_u32 s34, 28
	s_cselect_b64 s[4:5], -1, 0
	s_and_b64 s[34:35], s[4:5], exec
	s_cselect_b32 s38, 0, s38
	s_cselect_b32 s34, s23, s37
	s_cselect_b32 s35, s22, s36
	s_cselect_b32 s66, s21, s25
	s_cselect_b32 s67, s20, s24
	s_ashr_i32 s39, s38, 31
	s_lshl_b64 s[40:41], s[38:39], 18
	s_add_u32 s68, s67, s40
	s_addc_u32 s69, s66, s41
	s_add_u32 s40, s35, s40
	s_addc_u32 s41, s34, s41
	s_setprio 1
	s_waitcnt lgkmcnt(11)
	v_mfma_f32_16x16x32_bf16 v[158:161], v[162:165], v[214:217], v[158:161]
	v_mfma_f32_16x16x32_bf16 v[154:157], v[170:173], v[214:217], v[154:157]
	s_waitcnt lgkmcnt(10)
	v_mfma_f32_16x16x32_bf16 v[146:149], v[162:165], v[224:227], v[146:149]
	v_mfma_f32_16x16x32_bf16 v[138:141], v[170:173], v[224:227], v[138:141]
	s_waitcnt lgkmcnt(9)
	v_mfma_f32_16x16x32_bf16 v[130:133], v[162:165], v[232:235], v[130:133]
	v_mfma_f32_16x16x32_bf16 v[122:125], v[170:173], v[232:235], v[122:125]
	s_waitcnt lgkmcnt(8)
	v_mfma_f32_16x16x32_bf16 v[114:117], v[162:165], v[240:243], v[114:117]
	v_mfma_f32_16x16x32_bf16 v[106:109], v[170:173], v[240:243], v[106:109]
	ds_read_b64_tr_b16 v[162:163], v190 offset:16384
	ds_read_b64_tr_b16 v[164:165], v191 offset:16384
	ds_read_b64_tr_b16 v[170:171], v192 offset:16384
	ds_read_b64_tr_b16 v[172:173], v193 offset:16384
	s_waitcnt lgkmcnt(7)
	v_mfma_f32_16x16x32_bf16 v[158:161], v[166:169], v[218:221], v[158:161]
	v_mfma_f32_16x16x32_bf16 v[154:157], v[174:177], v[218:221], v[154:157]
	s_waitcnt lgkmcnt(6)
	v_mfma_f32_16x16x32_bf16 v[146:149], v[166:169], v[228:231], v[146:149]
	v_mfma_f32_16x16x32_bf16 v[138:141], v[174:177], v[228:231], v[138:141]
	s_waitcnt lgkmcnt(5)
	v_mfma_f32_16x16x32_bf16 v[130:133], v[166:169], v[236:239], v[130:133]
	v_mfma_f32_16x16x32_bf16 v[122:125], v[174:177], v[236:239], v[122:125]
	s_waitcnt lgkmcnt(4)
	v_mfma_f32_16x16x32_bf16 v[114:117], v[166:169], v[244:247], v[114:117]
	v_mfma_f32_16x16x32_bf16 v[106:109], v[174:177], v[244:247], v[106:109]
	ds_read_b64_tr_b16 v[166:167], v190 offset:24576
	ds_read_b64_tr_b16 v[168:169], v191 offset:24576
	ds_read_b64_tr_b16 v[174:175], v192 offset:24576
	ds_read_b64_tr_b16 v[176:177], v193 offset:24576
	s_waitcnt lgkmcnt(4)
	v_mfma_f32_16x16x32_bf16 v[150:153], v[162:165], v[214:217], v[150:153]
	v_mfma_f32_16x16x32_bf16 v[142:145], v[170:173], v[214:217], v[142:145]
	s_waitcnt vmcnt(9)
	v_cvt_pk_bf16_f32 v248, v2, v3
	v_cvt_pk_bf16_f32 v249, v4, v5
	ds_write_b64 v199, v[248:249]
	s_add_u32 s70, s40, 0x6000
	s_addc_u32 s71, s41, 0
	global_load_dwordx4 v[2:5], v189, s[70:71]
	v_mfma_f32_16x16x32_bf16 v[134:137], v[162:165], v[224:227], v[134:137]
	v_mfma_f32_16x16x32_bf16 v[126:129], v[170:173], v[224:227], v[126:129]
	s_waitcnt vmcnt(9)
	v_cvt_pk_bf16_f32 v248, v6, v7
	v_cvt_pk_bf16_f32 v249, v8, v9
	ds_write_b64 v200, v[248:249]
	s_add_u32 s72, s40, 0x4000
	s_addc_u32 s73, s41, 0
	global_load_dwordx4 v[6:9], v189, s[72:73]
	v_mfma_f32_16x16x32_bf16 v[118:121], v[162:165], v[232:235], v[118:121]
	v_mfma_f32_16x16x32_bf16 v[110:113], v[170:173], v[232:235], v[110:113]
	s_waitcnt vmcnt(9)
	v_cvt_pk_bf16_f32 v248, v10, v11
	v_cvt_pk_bf16_f32 v249, v12, v13
	ds_write_b64 v201, v[248:249]
	s_add_u32 s70, s68, 0x6000
	s_addc_u32 s71, s69, 0
	global_load_dwordx4 v[10:13], v189, s[70:71]
	v_mfma_f32_16x16x32_bf16 v[102:105], v[162:165], v[240:243], v[102:105]
	v_mfma_f32_16x16x32_bf16 v[98:101], v[170:173], v[240:243], v[98:101]
	s_waitcnt vmcnt(9)
	v_cvt_pk_bf16_f32 v248, v14, v15
	v_cvt_pk_bf16_f32 v249, v16, v17
	ds_write_b64 v202, v[248:249]
	s_add_u32 s72, s40, 0x2000
	s_addc_u32 s73, s41, 0
	global_load_dwordx4 v[14:17], v189, s[72:73]
	s_waitcnt lgkmcnt(4)
	v_mfma_f32_16x16x32_bf16 v[150:153], v[166:169], v[218:221], v[150:153]
	v_mfma_f32_16x16x32_bf16 v[142:145], v[174:177], v[218:221], v[142:145]
	s_waitcnt vmcnt(9)
	v_cvt_pk_bf16_f32 v248, v18, v19
	v_cvt_pk_bf16_f32 v249, v20, v21
	ds_write_b64 v203, v[248:249]
	s_add_u32 s70, s68, 0x4000
	s_addc_u32 s71, s69, 0
	global_load_dwordx4 v[18:21], v189, s[70:71]
	v_mfma_f32_16x16x32_bf16 v[134:137], v[166:169], v[228:231], v[134:137]
	v_mfma_f32_16x16x32_bf16 v[126:129], v[174:177], v[228:231], v[126:129]
	s_waitcnt vmcnt(9)
	v_cvt_pk_bf16_f32 v248, v22, v23
	v_cvt_pk_bf16_f32 v249, v24, v25
	ds_write_b64 v204, v[248:249]
	global_load_dwordx4 v[22:25], v189, s[40:41]
	v_mfma_f32_16x16x32_bf16 v[118:121], v[166:169], v[236:239], v[118:121]
	v_mfma_f32_16x16x32_bf16 v[110:113], v[174:177], v[236:239], v[110:113]
	s_waitcnt vmcnt(9)
	v_cvt_pk_bf16_f32 v248, v26, v27
	v_cvt_pk_bf16_f32 v249, v28, v29
	ds_write_b64 v205, v[248:249]
	s_add_u32 s70, s68, 0x2000
	s_addc_u32 s71, s69, 0
	global_load_dwordx4 v[26:29], v189, s[70:71]
	v_mfma_f32_16x16x32_bf16 v[102:105], v[166:169], v[244:247], v[102:105]
	v_mfma_f32_16x16x32_bf16 v[98:101], v[174:177], v[244:247], v[98:101]
	s_waitcnt vmcnt(9)
	v_cvt_pk_bf16_f32 v248, v34, v35
	v_cvt_pk_bf16_f32 v249, v36, v37
	ds_write_b64 v206, v[248:249]
	global_load_dwordx4 v[34:37], v189, s[68:69]
	s_setprio 0
	s_branch .Lswp_guE_tail
.Lswp_guO_half:
	ds_read_b64_tr_b16 v[162:163], v190 offset:32768
	ds_read_b64_tr_b16 v[164:165], v191 offset:32768
	ds_read_b64_tr_b16 v[170:171], v192 offset:32768
	ds_read_b64_tr_b16 v[172:173], v193 offset:32768
	ds_read_b128 v[214:217], v207 offset:32768
	ds_read_b128 v[224:227], v207 offset:34816
	ds_read_b128 v[232:235], v207 offset:36864
	ds_read_b128 v[240:243], v207 offset:38912
	ds_read_b64_tr_b16 v[166:167], v190 offset:40960
	ds_read_b64_tr_b16 v[168:169], v191 offset:40960
	ds_read_b64_tr_b16 v[174:175], v192 offset:40960
	ds_read_b64_tr_b16 v[176:177], v193 offset:40960
	ds_read_b128 v[218:221], v207 offset:33792
	ds_read_b128 v[228:231], v207 offset:35840
	ds_read_b128 v[236:239], v207 offset:37888
	ds_read_b128 v[244:247], v207 offset:39936
	s_lshl_b64 s[2:3], s[38:39], 18
	s_add_u32 s4, s2, 0x40000
	s_addc_u32 s5, s3, 0
	s_add_u32 s2, s67, s4
	s_addc_u32 s3, s66, s5
	s_add_u32 s4, s35, s4
	s_addc_u32 s5, s34, s5
	s_setprio 1
	s_waitcnt lgkmcnt(11)
	v_mfma_f32_16x16x32_bf16 v[158:161], v[162:165], v[214:217], v[158:161]
	v_mfma_f32_16x16x32_bf16 v[154:157], v[170:173], v[214:217], v[154:157]
	s_waitcnt lgkmcnt(10)
	v_mfma_f32_16x16x32_bf16 v[146:149], v[162:165], v[224:227], v[146:149]
	v_mfma_f32_16x16x32_bf16 v[138:141], v[170:173], v[224:227], v[138:141]
	s_waitcnt lgkmcnt(9)
	v_mfma_f32_16x16x32_bf16 v[130:133], v[162:165], v[232:235], v[130:133]
	v_mfma_f32_16x16x32_bf16 v[122:125], v[170:173], v[232:235], v[122:125]
	s_waitcnt lgkmcnt(8)
	v_mfma_f32_16x16x32_bf16 v[114:117], v[162:165], v[240:243], v[114:117]
	v_mfma_f32_16x16x32_bf16 v[106:109], v[170:173], v[240:243], v[106:109]
	ds_read_b64_tr_b16 v[162:163], v190 offset:49152
	ds_read_b64_tr_b16 v[164:165], v191 offset:49152
	ds_read_b64_tr_b16 v[170:171], v192 offset:49152
	ds_read_b64_tr_b16 v[172:173], v193 offset:49152
	s_waitcnt lgkmcnt(7)
	v_mfma_f32_16x16x32_bf16 v[158:161], v[166:169], v[218:221], v[158:161]
	v_mfma_f32_16x16x32_bf16 v[154:157], v[174:177], v[218:221], v[154:157]
	s_waitcnt lgkmcnt(6)
	v_mfma_f32_16x16x32_bf16 v[146:149], v[166:169], v[228:231], v[146:149]
	v_mfma_f32_16x16x32_bf16 v[138:141], v[174:177], v[228:231], v[138:141]
	s_waitcnt lgkmcnt(5)
	v_mfma_f32_16x16x32_bf16 v[130:133], v[166:169], v[236:239], v[130:133]
	v_mfma_f32_16x16x32_bf16 v[122:125], v[174:177], v[236:239], v[122:125]
	s_waitcnt lgkmcnt(4)
	v_mfma_f32_16x16x32_bf16 v[114:117], v[166:169], v[244:247], v[114:117]
	v_mfma_f32_16x16x32_bf16 v[106:109], v[174:177], v[244:247], v[106:109]
	ds_read_b64_tr_b16 v[166:167], v190 offset:57344
	ds_read_b64_tr_b16 v[168:169], v191 offset:57344
	ds_read_b64_tr_b16 v[174:175], v192 offset:57344
	ds_read_b64_tr_b16 v[176:177], v193 offset:57344
	s_waitcnt lgkmcnt(4)
	v_mfma_f32_16x16x32_bf16 v[150:153], v[162:165], v[214:217], v[150:153]
	v_mfma_f32_16x16x32_bf16 v[142:145], v[170:173], v[214:217], v[142:145]
	s_waitcnt vmcnt(9)
	v_cvt_pk_bf16_f32 v248, v2, v3
	v_cvt_pk_bf16_f32 v249, v4, v5
	ds_write_b64 v197, v[248:249] offset:16384
	global_load_dwordx4 v[2:5], v189, s[2:3]
	v_mfma_f32_16x16x32_bf16 v[134:137], v[162:165], v[224:227], v[134:137]
	v_mfma_f32_16x16x32_bf16 v[126:129], v[170:173], v[224:227], v[126:129]
	s_waitcnt vmcnt(9)
	v_cvt_pk_bf16_f32 v248, v6, v7
	v_cvt_pk_bf16_f32 v249, v8, v9
	ds_write_b64 v196, v[248:249] offset:16384
	global_load_dwordx4 v[6:9], v189, s[4:5]
	v_mfma_f32_16x16x32_bf16 v[118:121], v[162:165], v[232:235], v[118:121]
	v_mfma_f32_16x16x32_bf16 v[110:113], v[170:173], v[232:235], v[110:113]
	s_waitcnt vmcnt(9)
	v_cvt_pk_bf16_f32 v248, v10, v11
	v_cvt_pk_bf16_f32 v249, v12, v13
	ds_write_b64 v197, v[248:249]
	s_add_u32 s98, s2, 0x2000
	s_addc_u32 s99, s3, 0
	global_load_dwordx4 v[10:13], v189, s[98:99]
	v_mfma_f32_16x16x32_bf16 v[102:105], v[162:165], v[240:243], v[102:105]
	v_mfma_f32_16x16x32_bf16 v[98:101], v[170:173], v[240:243], v[98:101]
	s_waitcnt vmcnt(9)
	v_cvt_pk_bf16_f32 v248, v14, v15
	v_cvt_pk_bf16_f32 v249, v16, v17
	ds_write_b64 v195, v[248:249] offset:16384
	s_add_u32 s100, s4, 0x2000
	s_addc_u32 s101, s5, 0
	global_load_dwordx4 v[14:17], v189, s[100:101]
	s_waitcnt lgkmcnt(4)
	v_mfma_f32_16x16x32_bf16 v[150:153], v[166:169], v[218:221], v[150:153]
	v_mfma_f32_16x16x32_bf16 v[142:145], v[174:177], v[218:221], v[142:145]
	s_waitcnt vmcnt(9)
	v_cvt_pk_bf16_f32 v248, v18, v19
	v_cvt_pk_bf16_f32 v249, v20, v21
	ds_write_b64 v196, v[248:249]
	s_add_u32 s98, s2, 0x4000
	s_addc_u32 s99, s3, 0
	global_load_dwordx4 v[18:21], v189, s[98:99]
	v_mfma_f32_16x16x32_bf16 v[134:137], v[166:169], v[228:231], v[134:137]
	v_mfma_f32_16x16x32_bf16 v[126:129], v[174:177], v[228:231], v[126:129]
	s_waitcnt vmcnt(9)
	v_cvt_pk_bf16_f32 v248, v22, v23
	v_cvt_pk_bf16_f32 v249, v24, v25
	ds_write_b64 v194, v[248:249] offset:16384
	s_add_u32 s100, s4, 0x4000
	s_addc_u32 s101, s5, 0
	global_load_dwordx4 v[22:25], v189, s[100:101]
	v_mfma_f32_16x16x32_bf16 v[118:121], v[166:169], v[236:239], v[118:121]
	v_mfma_f32_16x16x32_bf16 v[110:113], v[174:177], v[236:239], v[110:113]
	s_waitcnt vmcnt(9)
	v_cvt_pk_bf16_f32 v248, v26, v27
	v_cvt_pk_bf16_f32 v249, v28, v29
	ds_write_b64 v195, v[248:249]
	s_add_u32 s98, s2, 0x6000
	s_addc_u32 s99, s3, 0
	global_load_dwordx4 v[26:29], v189, s[98:99]
	v_mfma_f32_16x16x32_bf16 v[102:105], v[166:169], v[244:247], v[102:105]
	v_mfma_f32_16x16x32_bf16 v[98:101], v[174:177], v[244:247], v[98:101]
	s_waitcnt vmcnt(9)
	v_cvt_pk_bf16_f32 v248, v34, v35
	v_cvt_pk_bf16_f32 v249, v36, v37
	ds_write_b64 v194, v[248:249]
	s_add_u32 s100, s4, 0x6000
	s_addc_u32 s101, s5, 0
	global_load_dwordx4 v[34:37], v189, s[100:101]
	s_setprio 0
	s_branch .Lswp_guO_tail

.LBB0_858:
	s_cmp_lg_u64 s[2:3], 0
	s_cbranch_scc1 .Lswp_dnE_half
	ds_read_b64_tr_b16 v[164:165], v190 offset:0
	ds_read_b64_tr_b16 v[166:167], v191 offset:0
	ds_read_b64_tr_b16 v[172:173], v192 offset:0
	ds_read_b64_tr_b16 v[174:175], v193 offset:0
	ds_read_b128 v[210:213], v207
	ds_read_b128 v[218:221], v207 offset:2048
	ds_read_b128 v[228:231], v207 offset:4096
	ds_read_b128 v[236:239], v207 offset:6144
	ds_read_b64_tr_b16 v[168:169], v190 offset:8192
	ds_read_b64_tr_b16 v[170:171], v191 offset:8192
	ds_read_b64_tr_b16 v[176:177], v192 offset:8192
	ds_read_b64_tr_b16 v[178:179], v193 offset:8192
	ds_read_b128 v[214:217], v207 offset:1024
	ds_read_b128 v[224:227], v207 offset:3072
	ds_read_b128 v[232:235], v207 offset:5120
	ds_read_b128 v[240:243], v207 offset:7168
	s_add_i32 s48, s48, 2
	s_cmp_eq_u32 s35, 12
	s_cselect_b32 s48, 0, s48
	s_cselect_b32 s77, s41, s23
	s_cselect_b32 s82, s40, s22
	s_cselect_b32 s35, s39, s47
	s_cselect_b32 s37, s38, s46
	s_cselect_b32 s43, s27, s45
	s_cselect_b32 s74, s26, s44
	s_cselect_b64 vcc, -1, 0
	s_ashr_i32 s49, s48, 31
	s_lshl_b64 s[50:51], s[48:49], 19
	s_add_u32 s72, s74, s50
	s_addc_u32 s73, s43, s51
	s_add_u32 s50, s37, s50
	s_addc_u32 s51, s35, s51
	s_setprio 1
	s_waitcnt lgkmcnt(11)
	v_mfma_f32_16x16x32_bf16 v[160:163], v[164:167], v[210:213], v[160:163]
	v_mfma_f32_16x16x32_bf16 v[156:159], v[172:175], v[210:213], v[156:159]
	s_waitcnt lgkmcnt(10)
	v_mfma_f32_16x16x32_bf16 v[152:155], v[164:167], v[218:221], v[152:155]
	v_mfma_f32_16x16x32_bf16 v[148:151], v[172:175], v[218:221], v[148:151]
	s_waitcnt lgkmcnt(9)
	v_mfma_f32_16x16x32_bf16 v[136:139], v[164:167], v[228:231], v[136:139]
	v_mfma_f32_16x16x32_bf16 v[132:135], v[172:175], v[228:231], v[132:135]
	s_waitcnt lgkmcnt(8)
	v_mfma_f32_16x16x32_bf16 v[120:123], v[164:167], v[236:239], v[120:123]
	v_mfma_f32_16x16x32_bf16 v[116:119], v[172:175], v[236:239], v[116:119]
	ds_read_b64_tr_b16 v[164:165], v190 offset:16384
	ds_read_b64_tr_b16 v[166:167], v191 offset:16384
	ds_read_b64_tr_b16 v[172:173], v192 offset:16384
	ds_read_b64_tr_b16 v[174:175], v193 offset:16384
	s_waitcnt lgkmcnt(7)
	v_mfma_f32_16x16x32_bf16 v[160:163], v[168:171], v[214:217], v[160:163]
	v_mfma_f32_16x16x32_bf16 v[156:159], v[176:179], v[214:217], v[156:159]
	s_waitcnt lgkmcnt(6)
	v_mfma_f32_16x16x32_bf16 v[152:155], v[168:171], v[224:227], v[152:155]
	v_mfma_f32_16x16x32_bf16 v[148:151], v[176:179], v[224:227], v[148:151]
	s_waitcnt lgkmcnt(5)
	v_mfma_f32_16x16x32_bf16 v[136:139], v[168:171], v[232:235], v[136:139]
	v_mfma_f32_16x16x32_bf16 v[132:135], v[176:179], v[232:235], v[132:135]
	s_waitcnt lgkmcnt(4)
	v_mfma_f32_16x16x32_bf16 v[120:123], v[168:171], v[240:243], v[120:123]
	v_mfma_f32_16x16x32_bf16 v[116:119], v[176:179], v[240:243], v[116:119]
	ds_read_b64_tr_b16 v[168:169], v190 offset:24576
	ds_read_b64_tr_b16 v[170:171], v191 offset:24576
	ds_read_b64_tr_b16 v[176:177], v192 offset:24576
	ds_read_b64_tr_b16 v[178:179], v193 offset:24576
	s_waitcnt lgkmcnt(4)
	v_mfma_f32_16x16x32_bf16 v[144:147], v[164:167], v[210:213], v[144:147]
	v_mfma_f32_16x16x32_bf16 v[140:143], v[172:175], v[210:213], v[140:143]
	ds_read_b128 v[210:213], v207 offset:16384
	v_mfma_f32_16x16x32_bf16 v[128:131], v[164:167], v[218:221], v[128:131]
	v_mfma_f32_16x16x32_bf16 v[124:127], v[172:175], v[218:221], v[124:127]
	ds_read_b128 v[218:221], v207 offset:18432
	v_mfma_f32_16x16x32_bf16 v[112:115], v[164:167], v[228:231], v[112:115]
	v_mfma_f32_16x16x32_bf16 v[108:111], v[172:175], v[228:231], v[108:111]
	ds_read_b128 v[228:231], v207 offset:20480
	v_mfma_f32_16x16x32_bf16 v[104:107], v[164:167], v[236:239], v[104:107]
	v_mfma_f32_16x16x32_bf16 v[100:103], v[172:175], v[236:239], v[100:103]
	ds_read_b128 v[236:239], v207 offset:22528
	ds_read_b64_tr_b16 v[164:165], v190 offset:0
	ds_read_b64_tr_b16 v[166:167], v191 offset:0
	ds_read_b64_tr_b16 v[172:173], v192 offset:0
	ds_read_b64_tr_b16 v[174:175], v193 offset:0
	s_waitcnt lgkmcnt(8)
	v_mfma_f32_16x16x32_bf16 v[144:147], v[168:171], v[214:217], v[144:147]
	v_mfma_f32_16x16x32_bf16 v[140:143], v[176:179], v[214:217], v[140:143]
	ds_read_b128 v[214:217], v207 offset:17408
	v_mfma_f32_16x16x32_bf16 v[128:131], v[168:171], v[224:227], v[128:131]
	v_mfma_f32_16x16x32_bf16 v[124:127], v[176:179], v[224:227], v[124:127]
	ds_read_b128 v[224:227], v207 offset:19456
	v_mfma_f32_16x16x32_bf16 v[112:115], v[168:171], v[232:235], v[112:115]
	v_mfma_f32_16x16x32_bf16 v[108:111], v[176:179], v[232:235], v[108:111]
	ds_read_b128 v[232:235], v207 offset:21504
	v_mfma_f32_16x16x32_bf16 v[104:107], v[168:171], v[240:243], v[104:107]
	v_mfma_f32_16x16x32_bf16 v[100:103], v[176:179], v[240:243], v[100:103]
	ds_read_b128 v[240:243], v207 offset:23552
	ds_read_b64_tr_b16 v[168:169], v190 offset:8192
	ds_read_b64_tr_b16 v[170:171], v191 offset:8192
	ds_read_b64_tr_b16 v[176:177], v192 offset:8192
	ds_read_b64_tr_b16 v[178:179], v193 offset:8192
	s_waitcnt lgkmcnt(8)
	v_mfma_f32_16x16x32_bf16 v[80:83], v[164:167], v[210:213], v[80:83]
	v_mfma_f32_16x16x32_bf16 v[68:71], v[172:175], v[210:213], v[68:71]
	v_mfma_f32_16x16x32_bf16 v[48:51], v[164:167], v[218:221], v[48:51]
	v_mfma_f32_16x16x32_bf16 v[44:47], v[172:175], v[218:221], v[44:47]
	v_mfma_f32_16x16x32_bf16 v[32:35], v[164:167], v[228:231], v[32:35]
	v_mfma_f32_16x16x32_bf16 v[28:31], v[172:175], v[228:231], v[28:31]
	v_mfma_f32_16x16x32_bf16 v[16:19], v[164:167], v[236:239], v[16:19]
	v_mfma_f32_16x16x32_bf16 v[12:15], v[172:175], v[236:239], v[12:15]
	ds_read_b64_tr_b16 v[164:165], v190 offset:16384
	ds_read_b64_tr_b16 v[166:167], v191 offset:16384
	ds_read_b64_tr_b16 v[172:173], v192 offset:16384
	ds_read_b64_tr_b16 v[174:175], v193 offset:16384
	s_waitcnt lgkmcnt(4)
	v_mfma_f32_16x16x32_bf16 v[80:83], v[168:171], v[214:217], v[80:83]
	v_mfma_f32_16x16x32_bf16 v[68:71], v[176:179], v[214:217], v[68:71]
	v_mfma_f32_16x16x32_bf16 v[48:51], v[168:171], v[224:227], v[48:51]
	v_mfma_f32_16x16x32_bf16 v[44:47], v[176:179], v[224:227], v[44:47]
	v_mfma_f32_16x16x32_bf16 v[32:35], v[168:171], v[232:235], v[32:35]
	v_mfma_f32_16x16x32_bf16 v[28:31], v[176:179], v[232:235], v[28:31]
	v_mfma_f32_16x16x32_bf16 v[16:19], v[168:171], v[240:243], v[16:19]
	v_mfma_f32_16x16x32_bf16 v[12:15], v[176:179], v[240:243], v[12:15]
	ds_read_b64_tr_b16 v[168:169], v190 offset:24576
	ds_read_b64_tr_b16 v[170:171], v191 offset:24576
	ds_read_b64_tr_b16 v[176:177], v192 offset:24576
	ds_read_b64_tr_b16 v[178:179], v193 offset:24576
	s_waitcnt lgkmcnt(4)
	v_mfma_f32_16x16x32_bf16 v[56:59], v[164:167], v[210:213], v[56:59]
	v_mfma_f32_16x16x32_bf16 v[52:55], v[172:175], v[210:213], v[52:55]
	s_waitcnt vmcnt(11)
	v_cvt_pk_bf16_f32 v244, v64, v65
	v_cvt_pk_bf16_f32 v245, v66, v67
	ds_write_b64 v199, v[244:245]
	s_add_u32 s78, s50, 0x8000
	s_addc_u32 s79, s51, 0
	global_load_dwordx4 v[64:67], v189, s[78:79]
	v_mfma_f32_16x16x32_bf16 v[40:43], v[164:167], v[218:221], v[40:43]
	v_mfma_f32_16x16x32_bf16 v[36:39], v[172:175], v[218:221], v[36:39]
	s_waitcnt vmcnt(11)
	v_cvt_pk_bf16_f32 v244, v60, v61
	v_cvt_pk_bf16_f32 v245, v62, v63
	ds_write_b64 v200, v[244:245]
	s_add_u32 s80, s50, 0xc000
	s_addc_u32 s81, s51, 0
	global_load_dwordx4 v[60:63], v189, s[80:81]
	v_mfma_f32_16x16x32_bf16 v[24:27], v[164:167], v[228:231], v[24:27]
	v_mfma_f32_16x16x32_bf16 v[20:23], v[172:175], v[228:231], v[20:23]
	s_waitcnt vmcnt(11)
	v_cvt_pk_bf16_f32 v244, v76, v77
	v_cvt_pk_bf16_f32 v245, v78, v79
	ds_write_b64 v201, v[244:245]
	s_add_u32 s78, s50, 0x4000
	s_addc_u32 s79, s51, 0
	global_load_dwordx4 v[76:79], v189, s[78:79]
	v_mfma_f32_16x16x32_bf16 v[8:11], v[164:167], v[236:239], v[8:11]
	v_mfma_f32_16x16x32_bf16 v[2:5], v[172:175], v[236:239], v[4:7]
	s_waitcnt vmcnt(11)
	v_cvt_pk_bf16_f32 v244, v72, v73
	v_cvt_pk_bf16_f32 v245, v74, v75
	ds_write_b64 v202, v[244:245]
	s_add_u32 s80, s72, 0xc000
	s_addc_u32 s81, s73, 0
	global_load_dwordx4 v[72:75], v189, s[80:81]
	s_waitcnt lgkmcnt(4)
	v_mfma_f32_16x16x32_bf16 v[56:59], v[168:171], v[214:217], v[56:59]
	v_mfma_f32_16x16x32_bf16 v[52:55], v[176:179], v[214:217], v[52:55]
	s_waitcnt vmcnt(11)
	v_cvt_pk_bf16_f32 v244, v88, v89
	v_cvt_pk_bf16_f32 v245, v90, v91
	ds_write_b64 v203, v[244:245]
	global_load_dwordx4 v[88:91], v189, s[50:51]
	v_mfma_f32_16x16x32_bf16 v[40:43], v[168:171], v[224:227], v[40:43]
	v_mfma_f32_16x16x32_bf16 v[36:39], v[176:179], v[224:227], v[36:39]
	s_waitcnt vmcnt(11)
	v_cvt_pk_bf16_f32 v244, v84, v85
	v_cvt_pk_bf16_f32 v245, v86, v87
	ds_write_b64 v204, v[244:245]
	s_add_u32 s80, s72, 0x8000
	s_addc_u32 s81, s73, 0
	global_load_dwordx4 v[84:87], v189, s[80:81]
	v_mfma_f32_16x16x32_bf16 v[24:27], v[168:171], v[232:235], v[24:27]
	v_mfma_f32_16x16x32_bf16 v[20:23], v[176:179], v[232:235], v[20:23]
	s_waitcnt vmcnt(11)
	v_cvt_pk_bf16_f32 v244, v96, v97
	v_cvt_pk_bf16_f32 v245, v98, v99
	ds_write_b64 v205, v[244:245]
	global_load_dwordx4 v[96:99], v189, s[72:73]
	v_mfma_f32_16x16x32_bf16 v[8:11], v[168:171], v[240:243], v[8:11]
	v_mfma_f32_16x16x32_bf16 v[4:7], v[176:179], v[240:243], v[2:5]
	s_waitcnt vmcnt(11)
	v_cvt_pk_bf16_f32 v244, v92, v93
	v_cvt_pk_bf16_f32 v245, v94, v95
	ds_write_b64 v206, v[244:245]
	s_add_u32 s80, s72, 0x4000
	s_addc_u32 s81, s73, 0
	global_load_dwordx4 v[92:95], v189, s[80:81]
	s_setprio 0

.LBB0_864:
	s_cmp_lg_u64 s[2:3], 0
	s_cbranch_scc1 .Lswp_dnO_half
	ds_read_b64_tr_b16 v[164:165], v190 offset:32768
	ds_read_b64_tr_b16 v[166:167], v191 offset:32768
	ds_read_b64_tr_b16 v[172:173], v192 offset:32768
	ds_read_b64_tr_b16 v[174:175], v193 offset:32768
	ds_read_b128 v[210:213], v207 offset:32768
	ds_read_b128 v[218:221], v207 offset:34816
	ds_read_b128 v[228:231], v207 offset:36864
	ds_read_b128 v[236:239], v207 offset:38912
	ds_read_b64_tr_b16 v[168:169], v190 offset:40960
	ds_read_b64_tr_b16 v[170:171], v191 offset:40960
	ds_read_b64_tr_b16 v[176:177], v192 offset:40960
	ds_read_b64_tr_b16 v[178:179], v193 offset:40960
	ds_read_b128 v[214:217], v207 offset:33792
	ds_read_b128 v[224:227], v207 offset:35840
	ds_read_b128 v[232:235], v207 offset:37888
	ds_read_b128 v[240:243], v207 offset:39936
	s_lshl_b64 s[2:3], s[48:49], 19
	s_add_u32 s48, s2, 0x80000
	s_addc_u32 s49, s3, 0
	s_add_u32 s2, s74, s48
	s_addc_u32 s3, s43, s49
	s_add_u32 s48, s37, s48
	s_addc_u32 s49, s35, s49
	s_setprio 1
	s_waitcnt lgkmcnt(11)
	v_mfma_f32_16x16x32_bf16 v[160:163], v[164:167], v[210:213], v[160:163]
	v_mfma_f32_16x16x32_bf16 v[156:159], v[172:175], v[210:213], v[156:159]
	s_waitcnt lgkmcnt(10)
	v_mfma_f32_16x16x32_bf16 v[152:155], v[164:167], v[218:221], v[152:155]
	v_mfma_f32_16x16x32_bf16 v[148:151], v[172:175], v[218:221], v[148:151]
	s_waitcnt lgkmcnt(9)
	v_mfma_f32_16x16x32_bf16 v[136:139], v[164:167], v[228:231], v[136:139]
	v_mfma_f32_16x16x32_bf16 v[132:135], v[172:175], v[228:231], v[132:135]
	s_waitcnt lgkmcnt(8)
	v_mfma_f32_16x16x32_bf16 v[120:123], v[164:167], v[236:239], v[120:123]
	v_mfma_f32_16x16x32_bf16 v[116:119], v[172:175], v[236:239], v[116:119]
	ds_read_b64_tr_b16 v[164:165], v190 offset:49152
	ds_read_b64_tr_b16 v[166:167], v191 offset:49152
	ds_read_b64_tr_b16 v[172:173], v192 offset:49152
	ds_read_b64_tr_b16 v[174:175], v193 offset:49152
	s_waitcnt lgkmcnt(7)
	v_mfma_f32_16x16x32_bf16 v[160:163], v[168:171], v[214:217], v[160:163]
	v_mfma_f32_16x16x32_bf16 v[156:159], v[176:179], v[214:217], v[156:159]
	s_waitcnt lgkmcnt(6)
	v_mfma_f32_16x16x32_bf16 v[152:155], v[168:171], v[224:227], v[152:155]
	v_mfma_f32_16x16x32_bf16 v[148:151], v[176:179], v[224:227], v[148:151]
	s_waitcnt lgkmcnt(5)
	v_mfma_f32_16x16x32_bf16 v[136:139], v[168:171], v[232:235], v[136:139]
	v_mfma_f32_16x16x32_bf16 v[132:135], v[176:179], v[232:235], v[132:135]
	s_waitcnt lgkmcnt(4)
	v_mfma_f32_16x16x32_bf16 v[120:123], v[168:171], v[240:243], v[120:123]
	v_mfma_f32_16x16x32_bf16 v[116:119], v[176:179], v[240:243], v[116:119]
	ds_read_b64_tr_b16 v[168:169], v190 offset:57344
	ds_read_b64_tr_b16 v[170:171], v191 offset:57344
	ds_read_b64_tr_b16 v[176:177], v192 offset:57344
	ds_read_b64_tr_b16 v[178:179], v193 offset:57344
	s_waitcnt lgkmcnt(4)
	v_mfma_f32_16x16x32_bf16 v[144:147], v[164:167], v[210:213], v[144:147]
	v_mfma_f32_16x16x32_bf16 v[140:143], v[172:175], v[210:213], v[140:143]
	ds_read_b128 v[210:213], v207 offset:49152
	v_mfma_f32_16x16x32_bf16 v[128:131], v[164:167], v[218:221], v[128:131]
	v_mfma_f32_16x16x32_bf16 v[124:127], v[172:175], v[218:221], v[124:127]
	ds_read_b128 v[218:221], v207 offset:51200
	v_mfma_f32_16x16x32_bf16 v[112:115], v[164:167], v[228:231], v[112:115]
	v_mfma_f32_16x16x32_bf16 v[108:111], v[172:175], v[228:231], v[108:111]
	ds_read_b128 v[228:231], v207 offset:53248
	v_mfma_f32_16x16x32_bf16 v[104:107], v[164:167], v[236:239], v[104:107]
	v_mfma_f32_16x16x32_bf16 v[100:103], v[172:175], v[236:239], v[100:103]
	ds_read_b128 v[236:239], v207 offset:55296
	ds_read_b64_tr_b16 v[164:165], v190 offset:32768
	ds_read_b64_tr_b16 v[166:167], v191 offset:32768
	ds_read_b64_tr_b16 v[172:173], v192 offset:32768
	ds_read_b64_tr_b16 v[174:175], v193 offset:32768
	s_waitcnt lgkmcnt(8)
	v_mfma_f32_16x16x32_bf16 v[144:147], v[168:171], v[214:217], v[144:147]
	v_mfma_f32_16x16x32_bf16 v[140:143], v[176:179], v[214:217], v[140:143]
	ds_read_b128 v[214:217], v207 offset:50176
	v_mfma_f32_16x16x32_bf16 v[128:131], v[168:171], v[224:227], v[128:131]
	v_mfma_f32_16x16x32_bf16 v[124:127], v[176:179], v[224:227], v[124:127]
	ds_read_b128 v[224:227], v207 offset:52224
	v_mfma_f32_16x16x32_bf16 v[112:115], v[168:171], v[232:235], v[112:115]
	v_mfma_f32_16x16x32_bf16 v[108:111], v[176:179], v[232:235], v[108:111]
	ds_read_b128 v[232:235], v207 offset:54272
	v_mfma_f32_16x16x32_bf16 v[104:107], v[168:171], v[240:243], v[104:107]
	v_mfma_f32_16x16x32_bf16 v[100:103], v[176:179], v[240:243], v[100:103]
	ds_read_b128 v[240:243], v207 offset:56320
	ds_read_b64_tr_b16 v[168:169], v190 offset:40960
	ds_read_b64_tr_b16 v[170:171], v191 offset:40960
	ds_read_b64_tr_b16 v[176:177], v192 offset:40960
	ds_read_b64_tr_b16 v[178:179], v193 offset:40960
	s_waitcnt lgkmcnt(8)
	v_mfma_f32_16x16x32_bf16 v[80:83], v[164:167], v[210:213], v[80:83]
	v_mfma_f32_16x16x32_bf16 v[68:71], v[172:175], v[210:213], v[68:71]
	v_mfma_f32_16x16x32_bf16 v[48:51], v[164:167], v[218:221], v[48:51]
	v_mfma_f32_16x16x32_bf16 v[44:47], v[172:175], v[218:221], v[44:47]
	v_mfma_f32_16x16x32_bf16 v[32:35], v[164:167], v[228:231], v[32:35]
	v_mfma_f32_16x16x32_bf16 v[28:31], v[172:175], v[228:231], v[28:31]
	v_mfma_f32_16x16x32_bf16 v[16:19], v[164:167], v[236:239], v[16:19]
	v_mfma_f32_16x16x32_bf16 v[12:15], v[172:175], v[236:239], v[12:15]
	ds_read_b64_tr_b16 v[164:165], v190 offset:49152
	ds_read_b64_tr_b16 v[166:167], v191 offset:49152
	ds_read_b64_tr_b16 v[172:173], v192 offset:49152
	ds_read_b64_tr_b16 v[174:175], v193 offset:49152
	s_waitcnt lgkmcnt(4)
	v_mfma_f32_16x16x32_bf16 v[80:83], v[168:171], v[214:217], v[80:83]
	v_mfma_f32_16x16x32_bf16 v[68:71], v[176:179], v[214:217], v[68:71]
	v_mfma_f32_16x16x32_bf16 v[48:51], v[168:171], v[224:227], v[48:51]
	v_mfma_f32_16x16x32_bf16 v[44:47], v[176:179], v[224:227], v[44:47]
	v_mfma_f32_16x16x32_bf16 v[32:35], v[168:171], v[232:235], v[32:35]
	v_mfma_f32_16x16x32_bf16 v[28:31], v[176:179], v[232:235], v[28:31]
	v_mfma_f32_16x16x32_bf16 v[16:19], v[168:171], v[240:243], v[16:19]
	v_mfma_f32_16x16x32_bf16 v[12:15], v[176:179], v[240:243], v[12:15]
	ds_read_b64_tr_b16 v[168:169], v190 offset:57344
	ds_read_b64_tr_b16 v[170:171], v191 offset:57344
	ds_read_b64_tr_b16 v[176:177], v192 offset:57344
	ds_read_b64_tr_b16 v[178:179], v193 offset:57344
	s_waitcnt lgkmcnt(4)
	v_mfma_f32_16x16x32_bf16 v[56:59], v[164:167], v[210:213], v[56:59]
	v_mfma_f32_16x16x32_bf16 v[52:55], v[172:175], v[210:213], v[52:55]
	s_waitcnt vmcnt(9)
	v_cvt_pk_bf16_f32 v244, v64, v65
	v_cvt_pk_bf16_f32 v245, v66, v67
	ds_write_b64 v196, v[244:245] offset:16384
	global_load_dwordx4 v[64:67], v189, s[2:3]
	v_mfma_f32_16x16x32_bf16 v[40:43], v[164:167], v[218:221], v[40:43]
	v_mfma_f32_16x16x32_bf16 v[36:39], v[172:175], v[218:221], v[36:39]
	s_waitcnt vmcnt(9)
	v_cvt_pk_bf16_f32 v244, v60, v61
	v_cvt_pk_bf16_f32 v245, v62, v63
	ds_write_b64 v197, v[244:245] offset:16384
	global_load_dwordx4 v[60:63], v189, s[48:49]
	v_mfma_f32_16x16x32_bf16 v[24:27], v[164:167], v[228:231], v[24:27]
	v_mfma_f32_16x16x32_bf16 v[20:23], v[172:175], v[228:231], v[20:23]
	s_waitcnt vmcnt(9)
	v_cvt_pk_bf16_f32 v244, v76, v77
	v_cvt_pk_bf16_f32 v245, v78, v79
	ds_write_b64 v195, v[244:245] offset:16384
	s_add_u32 s98, s2, 0x4000
	s_addc_u32 s99, s3, 0
	global_load_dwordx4 v[76:79], v189, s[98:99]
	v_mfma_f32_16x16x32_bf16 v[8:11], v[164:167], v[236:239], v[8:11]
	v_mfma_f32_16x16x32_bf16 v[2:5], v[172:175], v[236:239], v[4:7]
	s_waitcnt vmcnt(9)
	v_cvt_pk_bf16_f32 v244, v72, v73
	v_cvt_pk_bf16_f32 v245, v74, v75
	ds_write_b64 v197, v[244:245]
	s_add_u32 s100, s48, 0x4000
	s_addc_u32 s101, s49, 0
	global_load_dwordx4 v[72:75], v189, s[100:101]
	s_waitcnt lgkmcnt(4)
	v_mfma_f32_16x16x32_bf16 v[56:59], v[168:171], v[214:217], v[56:59]
	v_mfma_f32_16x16x32_bf16 v[52:55], v[176:179], v[214:217], v[52:55]
	s_waitcnt vmcnt(9)
	v_cvt_pk_bf16_f32 v244, v88, v89
	v_cvt_pk_bf16_f32 v245, v90, v91
	ds_write_b64 v194, v[244:245] offset:16384
	s_add_u32 s98, s2, 0x8000
	s_addc_u32 s99, s3, 0
	global_load_dwordx4 v[88:91], v189, s[98:99]
	v_mfma_f32_16x16x32_bf16 v[40:43], v[168:171], v[224:227], v[40:43]
	v_mfma_f32_16x16x32_bf16 v[36:39], v[176:179], v[224:227], v[36:39]
	s_waitcnt vmcnt(9)
	v_cvt_pk_bf16_f32 v244, v84, v85
	v_cvt_pk_bf16_f32 v245, v86, v87
	ds_write_b64 v196, v[244:245]
	s_add_u32 s100, s48, 0x8000
	s_addc_u32 s101, s49, 0
	global_load_dwordx4 v[84:87], v189, s[100:101]
	v_mfma_f32_16x16x32_bf16 v[24:27], v[168:171], v[232:235], v[24:27]
	v_mfma_f32_16x16x32_bf16 v[20:23], v[176:179], v[232:235], v[20:23]
	s_waitcnt vmcnt(9)
	v_cvt_pk_bf16_f32 v244, v96, v97
	v_cvt_pk_bf16_f32 v245, v98, v99
	ds_write_b64 v194, v[244:245]
	s_add_u32 s98, s2, 0xc000
	s_addc_u32 s99, s3, 0
	global_load_dwordx4 v[96:99], v189, s[98:99]
	v_mfma_f32_16x16x32_bf16 v[8:11], v[168:171], v[240:243], v[8:11]
	v_mfma_f32_16x16x32_bf16 v[4:7], v[176:179], v[240:243], v[2:5]
	s_waitcnt vmcnt(9)
	v_cvt_pk_bf16_f32 v244, v92, v93
	v_cvt_pk_bf16_f32 v245, v94, v95
	ds_write_b64 v195, v[244:245]
	s_add_u32 s100, s48, 0xc000
	s_addc_u32 s101, s49, 0
	global_load_dwordx4 v[92:95], v189, s[100:101]
	s_setprio 0

.Lswp_dnE_half:
	ds_read_b64_tr_b16 v[164:165], v190 offset:0
	ds_read_b64_tr_b16 v[166:167], v191 offset:0
	ds_read_b64_tr_b16 v[172:173], v192 offset:0
	ds_read_b64_tr_b16 v[174:175], v193 offset:0
	ds_read_b128 v[210:213], v207
	ds_read_b128 v[218:221], v207 offset:2048
	ds_read_b128 v[228:231], v207 offset:4096
	ds_read_b128 v[236:239], v207 offset:6144
	ds_read_b64_tr_b16 v[168:169], v190 offset:8192
	ds_read_b64_tr_b16 v[170:171], v191 offset:8192
	ds_read_b64_tr_b16 v[176:177], v192 offset:8192
	ds_read_b64_tr_b16 v[178:179], v193 offset:8192
	ds_read_b128 v[214:217], v207 offset:1024
	ds_read_b128 v[224:227], v207 offset:3072
	ds_read_b128 v[232:235], v207 offset:5120
	ds_read_b128 v[240:243], v207 offset:7168
	s_add_i32 s48, s48, 2
	s_cmp_eq_u32 s35, 12
	s_cselect_b32 s48, 0, s48
	s_cselect_b32 s77, s41, s23
	s_cselect_b32 s82, s40, s22
	s_cselect_b32 s35, s39, s47
	s_cselect_b32 s37, s38, s46
	s_cselect_b32 s43, s27, s45
	s_cselect_b32 s74, s26, s44
	s_cselect_b64 vcc, -1, 0
	s_ashr_i32 s49, s48, 31
	s_lshl_b64 s[50:51], s[48:49], 19
	s_add_u32 s72, s74, s50
	s_addc_u32 s73, s43, s51
	s_add_u32 s50, s37, s50
	s_addc_u32 s51, s35, s51
	s_setprio 1
	s_waitcnt lgkmcnt(11)
	v_mfma_f32_16x16x32_bf16 v[160:163], v[164:167], v[210:213], v[160:163]
	v_mfma_f32_16x16x32_bf16 v[156:159], v[172:175], v[210:213], v[156:159]
	s_waitcnt lgkmcnt(10)
	v_mfma_f32_16x16x32_bf16 v[152:155], v[164:167], v[218:221], v[152:155]
	v_mfma_f32_16x16x32_bf16 v[148:151], v[172:175], v[218:221], v[148:151]
	s_waitcnt lgkmcnt(9)
	v_mfma_f32_16x16x32_bf16 v[136:139], v[164:167], v[228:231], v[136:139]
	v_mfma_f32_16x16x32_bf16 v[132:135], v[172:175], v[228:231], v[132:135]
	s_waitcnt lgkmcnt(8)
	v_mfma_f32_16x16x32_bf16 v[120:123], v[164:167], v[236:239], v[120:123]
	v_mfma_f32_16x16x32_bf16 v[116:119], v[172:175], v[236:239], v[116:119]
	ds_read_b64_tr_b16 v[164:165], v190 offset:16384
	ds_read_b64_tr_b16 v[166:167], v191 offset:16384
	ds_read_b64_tr_b16 v[172:173], v192 offset:16384
	ds_read_b64_tr_b16 v[174:175], v193 offset:16384
	s_waitcnt lgkmcnt(7)
	v_mfma_f32_16x16x32_bf16 v[160:163], v[168:171], v[214:217], v[160:163]
	v_mfma_f32_16x16x32_bf16 v[156:159], v[176:179], v[214:217], v[156:159]
	s_waitcnt lgkmcnt(6)
	v_mfma_f32_16x16x32_bf16 v[152:155], v[168:171], v[224:227], v[152:155]
	v_mfma_f32_16x16x32_bf16 v[148:151], v[176:179], v[224:227], v[148:151]
	s_waitcnt lgkmcnt(5)
	v_mfma_f32_16x16x32_bf16 v[136:139], v[168:171], v[232:235], v[136:139]
	v_mfma_f32_16x16x32_bf16 v[132:135], v[176:179], v[232:235], v[132:135]
	s_waitcnt lgkmcnt(4)
	v_mfma_f32_16x16x32_bf16 v[120:123], v[168:171], v[240:243], v[120:123]
	v_mfma_f32_16x16x32_bf16 v[116:119], v[176:179], v[240:243], v[116:119]
	ds_read_b64_tr_b16 v[168:169], v190 offset:24576
	ds_read_b64_tr_b16 v[170:171], v191 offset:24576
	ds_read_b64_tr_b16 v[176:177], v192 offset:24576
	ds_read_b64_tr_b16 v[178:179], v193 offset:24576
	s_waitcnt lgkmcnt(4)
	v_mfma_f32_16x16x32_bf16 v[144:147], v[164:167], v[210:213], v[144:147]
	v_mfma_f32_16x16x32_bf16 v[140:143], v[172:175], v[210:213], v[140:143]
	s_waitcnt vmcnt(9)
	v_cvt_pk_bf16_f32 v244, v64, v65
	v_cvt_pk_bf16_f32 v245, v66, v67
	ds_write_b64 v199, v[244:245]
	s_add_u32 s78, s50, 0x8000
	s_addc_u32 s79, s51, 0
	global_load_dwordx4 v[64:67], v189, s[78:79]
	v_mfma_f32_16x16x32_bf16 v[128:131], v[164:167], v[218:221], v[128:131]
	v_mfma_f32_16x16x32_bf16 v[124:127], v[172:175], v[218:221], v[124:127]
	s_waitcnt vmcnt(9)
	v_cvt_pk_bf16_f32 v244, v60, v61
	v_cvt_pk_bf16_f32 v245, v62, v63
	ds_write_b64 v200, v[244:245]
	s_add_u32 s80, s50, 0xc000
	s_addc_u32 s81, s51, 0
	global_load_dwordx4 v[60:63], v189, s[80:81]
	v_mfma_f32_16x16x32_bf16 v[112:115], v[164:167], v[228:231], v[112:115]
	v_mfma_f32_16x16x32_bf16 v[108:111], v[172:175], v[228:231], v[108:111]
	s_waitcnt vmcnt(9)
	v_cvt_pk_bf16_f32 v244, v76, v77
	v_cvt_pk_bf16_f32 v245, v78, v79
	ds_write_b64 v201, v[244:245]
	s_add_u32 s78, s50, 0x4000
	s_addc_u32 s79, s51, 0
	global_load_dwordx4 v[76:79], v189, s[78:79]
	v_mfma_f32_16x16x32_bf16 v[104:107], v[164:167], v[236:239], v[104:107]
	v_mfma_f32_16x16x32_bf16 v[100:103], v[172:175], v[236:239], v[100:103]
	s_waitcnt vmcnt(9)
	v_cvt_pk_bf16_f32 v244, v72, v73
	v_cvt_pk_bf16_f32 v245, v74, v75
	ds_write_b64 v202, v[244:245]
	s_add_u32 s80, s72, 0xc000
	s_addc_u32 s81, s73, 0
	global_load_dwordx4 v[72:75], v189, s[80:81]
	s_waitcnt lgkmcnt(4)
	v_mfma_f32_16x16x32_bf16 v[144:147], v[168:171], v[214:217], v[144:147]
	v_mfma_f32_16x16x32_bf16 v[140:143], v[176:179], v[214:217], v[140:143]
	s_waitcnt vmcnt(9)
	v_cvt_pk_bf16_f32 v244, v88, v89
	v_cvt_pk_bf16_f32 v245, v90, v91
	ds_write_b64 v203, v[244:245]
	global_load_dwordx4 v[88:91], v189, s[50:51]
	v_mfma_f32_16x16x32_bf16 v[128:131], v[168:171], v[224:227], v[128:131]
	v_mfma_f32_16x16x32_bf16 v[124:127], v[176:179], v[224:227], v[124:127]
	s_waitcnt vmcnt(9)
	v_cvt_pk_bf16_f32 v244, v84, v85
	v_cvt_pk_bf16_f32 v245, v86, v87
	ds_write_b64 v204, v[244:245]
	s_add_u32 s80, s72, 0x8000
	s_addc_u32 s81, s73, 0
	global_load_dwordx4 v[84:87], v189, s[80:81]
	v_mfma_f32_16x16x32_bf16 v[112:115], v[168:171], v[232:235], v[112:115]
	v_mfma_f32_16x16x32_bf16 v[108:111], v[176:179], v[232:235], v[108:111]
	s_waitcnt vmcnt(9)
	v_cvt_pk_bf16_f32 v244, v96, v97
	v_cvt_pk_bf16_f32 v245, v98, v99
	ds_write_b64 v205, v[244:245]
	global_load_dwordx4 v[96:99], v189, s[72:73]
	v_mfma_f32_16x16x32_bf16 v[104:107], v[168:171], v[240:243], v[104:107]
	v_mfma_f32_16x16x32_bf16 v[100:103], v[176:179], v[240:243], v[100:103]
	s_waitcnt vmcnt(9)
	v_cvt_pk_bf16_f32 v244, v92, v93
	v_cvt_pk_bf16_f32 v245, v94, v95
	ds_write_b64 v206, v[244:245]
	s_add_u32 s80, s72, 0x4000
	s_addc_u32 s81, s73, 0
	global_load_dwordx4 v[92:95], v189, s[80:81]
	s_setprio 0
	s_branch .Lswp_dnE_tail
.Lswp_dnO_half:
	ds_read_b64_tr_b16 v[164:165], v190 offset:32768
	ds_read_b64_tr_b16 v[166:167], v191 offset:32768
	ds_read_b64_tr_b16 v[172:173], v192 offset:32768
	ds_read_b64_tr_b16 v[174:175], v193 offset:32768
	ds_read_b128 v[210:213], v207 offset:32768
	ds_read_b128 v[218:221], v207 offset:34816
	ds_read_b128 v[228:231], v207 offset:36864
	ds_read_b128 v[236:239], v207 offset:38912
	ds_read_b64_tr_b16 v[168:169], v190 offset:40960
	ds_read_b64_tr_b16 v[170:171], v191 offset:40960
	ds_read_b64_tr_b16 v[176:177], v192 offset:40960
	ds_read_b64_tr_b16 v[178:179], v193 offset:40960
	ds_read_b128 v[214:217], v207 offset:33792
	ds_read_b128 v[224:227], v207 offset:35840
	ds_read_b128 v[232:235], v207 offset:37888
	ds_read_b128 v[240:243], v207 offset:39936
	s_lshl_b64 s[2:3], s[48:49], 19
	s_add_u32 s48, s2, 0x80000
	s_addc_u32 s49, s3, 0
	s_add_u32 s2, s74, s48
	s_addc_u32 s3, s43, s49
	s_add_u32 s48, s37, s48
	s_addc_u32 s49, s35, s49
	s_setprio 1
	s_waitcnt lgkmcnt(11)
	v_mfma_f32_16x16x32_bf16 v[160:163], v[164:167], v[210:213], v[160:163]
	v_mfma_f32_16x16x32_bf16 v[156:159], v[172:175], v[210:213], v[156:159]
	s_waitcnt lgkmcnt(10)
	v_mfma_f32_16x16x32_bf16 v[152:155], v[164:167], v[218:221], v[152:155]
	v_mfma_f32_16x16x32_bf16 v[148:151], v[172:175], v[218:221], v[148:151]
	s_waitcnt lgkmcnt(9)
	v_mfma_f32_16x16x32_bf16 v[136:139], v[164:167], v[228:231], v[136:139]
	v_mfma_f32_16x16x32_bf16 v[132:135], v[172:175], v[228:231], v[132:135]
	s_waitcnt lgkmcnt(8)
	v_mfma_f32_16x16x32_bf16 v[120:123], v[164:167], v[236:239], v[120:123]
	v_mfma_f32_16x16x32_bf16 v[116:119], v[172:175], v[236:239], v[116:119]
	ds_read_b64_tr_b16 v[164:165], v190 offset:49152
	ds_read_b64_tr_b16 v[166:167], v191 offset:49152
	ds_read_b64_tr_b16 v[172:173], v192 offset:49152
	ds_read_b64_tr_b16 v[174:175], v193 offset:49152
	s_waitcnt lgkmcnt(7)
	v_mfma_f32_16x16x32_bf16 v[160:163], v[168:171], v[214:217], v[160:163]
	v_mfma_f32_16x16x32_bf16 v[156:159], v[176:179], v[214:217], v[156:159]
	s_waitcnt lgkmcnt(6)
	v_mfma_f32_16x16x32_bf16 v[152:155], v[168:171], v[224:227], v[152:155]
	v_mfma_f32_16x16x32_bf16 v[148:151], v[176:179], v[224:227], v[148:151]
	s_waitcnt lgkmcnt(5)
	v_mfma_f32_16x16x32_bf16 v[136:139], v[168:171], v[232:235], v[136:139]
	v_mfma_f32_16x16x32_bf16 v[132:135], v[176:179], v[232:235], v[132:135]
	s_waitcnt lgkmcnt(4)
	v_mfma_f32_16x16x32_bf16 v[120:123], v[168:171], v[240:243], v[120:123]
	v_mfma_f32_16x16x32_bf16 v[116:119], v[176:179], v[240:243], v[116:119]
	ds_read_b64_tr_b16 v[168:169], v190 offset:57344
	ds_read_b64_tr_b16 v[170:171], v191 offset:57344
	ds_read_b64_tr_b16 v[176:177], v192 offset:57344
	ds_read_b64_tr_b16 v[178:179], v193 offset:57344
	s_waitcnt lgkmcnt(4)
	v_mfma_f32_16x16x32_bf16 v[144:147], v[164:167], v[210:213], v[144:147]
	v_mfma_f32_16x16x32_bf16 v[140:143], v[172:175], v[210:213], v[140:143]
	s_waitcnt vmcnt(9)
	v_cvt_pk_bf16_f32 v244, v64, v65
	v_cvt_pk_bf16_f32 v245, v66, v67
	ds_write_b64 v196, v[244:245] offset:16384
	global_load_dwordx4 v[64:67], v189, s[2:3]
	v_mfma_f32_16x16x32_bf16 v[128:131], v[164:167], v[218:221], v[128:131]
	v_mfma_f32_16x16x32_bf16 v[124:127], v[172:175], v[218:221], v[124:127]
	s_waitcnt vmcnt(9)
	v_cvt_pk_bf16_f32 v244, v60, v61
	v_cvt_pk_bf16_f32 v245, v62, v63
	ds_write_b64 v197, v[244:245] offset:16384
	global_load_dwordx4 v[60:63], v189, s[48:49]
	v_mfma_f32_16x16x32_bf16 v[112:115], v[164:167], v[228:231], v[112:115]
	v_mfma_f32_16x16x32_bf16 v[108:111], v[172:175], v[228:231], v[108:111]
	s_waitcnt vmcnt(9)
	v_cvt_pk_bf16_f32 v244, v76, v77
	v_cvt_pk_bf16_f32 v245, v78, v79
	ds_write_b64 v195, v[244:245] offset:16384
	s_add_u32 s98, s2, 0x4000
	s_addc_u32 s99, s3, 0
	global_load_dwordx4 v[76:79], v189, s[98:99]
	v_mfma_f32_16x16x32_bf16 v[104:107], v[164:167], v[236:239], v[104:107]
	v_mfma_f32_16x16x32_bf16 v[100:103], v[172:175], v[236:239], v[100:103]
	s_waitcnt vmcnt(9)
	v_cvt_pk_bf16_f32 v244, v72, v73
	v_cvt_pk_bf16_f32 v245, v74, v75
	ds_write_b64 v197, v[244:245]
	s_add_u32 s100, s48, 0x4000
	s_addc_u32 s101, s49, 0
	global_load_dwordx4 v[72:75], v189, s[100:101]
	s_waitcnt lgkmcnt(4)
	v_mfma_f32_16x16x32_bf16 v[144:147], v[168:171], v[214:217], v[144:147]
	v_mfma_f32_16x16x32_bf16 v[140:143], v[176:179], v[214:217], v[140:143]
	s_waitcnt vmcnt(9)
	v_cvt_pk_bf16_f32 v244, v88, v89
	v_cvt_pk_bf16_f32 v245, v90, v91
	ds_write_b64 v194, v[244:245] offset:16384
	s_add_u32 s98, s2, 0x8000
	s_addc_u32 s99, s3, 0
	global_load_dwordx4 v[88:91], v189, s[98:99]
	v_mfma_f32_16x16x32_bf16 v[128:131], v[168:171], v[224:227], v[128:131]
	v_mfma_f32_16x16x32_bf16 v[124:127], v[176:179], v[224:227], v[124:127]
	s_waitcnt vmcnt(9)
	v_cvt_pk_bf16_f32 v244, v84, v85
	v_cvt_pk_bf16_f32 v245, v86, v87
	ds_write_b64 v196, v[244:245]
	s_add_u32 s100, s48, 0x8000
	s_addc_u32 s101, s49, 0
	global_load_dwordx4 v[84:87], v189, s[100:101]
	v_mfma_f32_16x16x32_bf16 v[112:115], v[168:171], v[232:235], v[112:115]
	v_mfma_f32_16x16x32_bf16 v[108:111], v[176:179], v[232:235], v[108:111]
	s_waitcnt vmcnt(9)
	v_cvt_pk_bf16_f32 v244, v96, v97
	v_cvt_pk_bf16_f32 v245, v98, v99
	ds_write_b64 v194, v[244:245]
	s_add_u32 s98, s2, 0xc000
	s_addc_u32 s99, s3, 0
	global_load_dwordx4 v[96:99], v189, s[98:99]
	v_mfma_f32_16x16x32_bf16 v[104:107], v[168:171], v[240:243], v[104:107]
	v_mfma_f32_16x16x32_bf16 v[100:103], v[176:179], v[240:243], v[100:103]
	s_waitcnt vmcnt(9)
	v_cvt_pk_bf16_f32 v244, v92, v93
	v_cvt_pk_bf16_f32 v245, v94, v95
	ds_write_b64 v195, v[244:245]
	s_add_u32 s100, s48, 0xc000
	s_addc_u32 s101, s49, 0
	global_load_dwordx4 v[92:95], v189, s[100:101]
	s_setprio 0
	s_branch .Lswp_dnO_tail
